# moe_stagger step 38 (8 groups x ~1.0us) instead of 56
# speedup vs baseline: 1.0010x; 1.0010x over previous
.Lstg_loop:
	s_sleep 38
	s_add_i32 s98, s98, -1
	s_cmp_lg_u32 s98, 0
	s_cbranch_scc1 .Lstg_loop
